# attention far-bucket test: list reads prefetched at loop top and the wave-uniform test taken from VCC directly (no cndmask/readfirstlane); on top of v26
# baseline (speedup 1.0000x reference)
.LBB0_720:
	s_add_i32 s12, s47, -2
	s_lshr_b32 s42, s12, 2
	s_add_i32 s42, s42, s44
	s_and_b32 s34, s12, 2
	s_lshl_b32 s12, s42, 9
	s_add_i32 s43, s12, 0
	s_lshl_b32 s12, s34, 7
	s_add_i32 s43, s43, s12
	v_mov_b32_e32 v200, s43
	ds_read_u16 v201, v200 offset:33022
	ds_read_u16 v200, v200 offset:32894
	v_lshl_add_u32 v90, v233, 1, s43
	ds_read_u16 v102, v90 offset:32896
	ds_read_u16 v106, v90 offset:32912
	ds_read_u16 v110, v90 offset:32928
	ds_read_u16 v114, v90 offset:32944
	ds_read_u16 v86, v90 offset:32960
	ds_read_u16 v91, v90 offset:32976
	ds_read_u16 v94, v90 offset:32992
	ds_read_u16 v98, v90 offset:33008
	s_waitcnt lgkmcnt(7)
	v_lshl_add_u32 v118, v102, 9, v196
	v_lshlrev_b32_e32 v0, 9, v102
	v_lshl_add_u64 v[102:103], v[212:213], 0, v[0:1]
	s_waitcnt lgkmcnt(6)
	v_lshl_add_u32 v119, v106, 9, v197
	v_lshlrev_b32_e32 v0, 9, v106
	v_lshl_add_u64 v[106:107], v[212:213], 0, v[0:1]
	s_waitcnt lgkmcnt(5)
	v_lshl_add_u32 v120, v110, 9, v196
	v_lshlrev_b32_e32 v0, 9, v110
	v_lshl_add_u64 v[110:111], v[212:213], 0, v[0:1]
	s_waitcnt lgkmcnt(4)
	v_lshl_add_u32 v121, v114, 9, v197
	v_lshlrev_b32_e32 v0, 9, v114
	v_lshl_add_u64 v[114:115], v[212:213], 0, v[0:1]
	s_waitcnt lgkmcnt(3)
	v_lshl_add_u32 v122, v86, 9, v196
	v_lshlrev_b32_e32 v0, 9, v86
	v_lshl_add_u64 v[86:87], v[212:213], 0, v[0:1]
	s_waitcnt lgkmcnt(2)
	v_lshl_add_u32 v123, v91, 9, v197
	v_lshlrev_b32_e32 v0, 9, v91
	v_lshl_add_u64 v[90:91], v[212:213], 0, v[0:1]
	s_waitcnt lgkmcnt(1)
	v_lshl_add_u32 v124, v94, 9, v196
	v_lshlrev_b32_e32 v0, 9, v94
	v_lshl_add_u64 v[94:95], v[212:213], 0, v[0:1]
	s_waitcnt lgkmcnt(0)
	v_lshl_add_u32 v125, v98, 9, v197
	v_lshlrev_b32_e32 v0, 9, v98
	v_lshl_add_u64 v[98:99], v[212:213], 0, v[0:1]
	global_load_dwordx4 v[102:105], v[102:103], off offset:128
	s_nop 0
	global_load_dwordx4 v[106:109], v[106:107], off offset:128
	s_nop 0
	global_load_dwordx4 v[110:113], v[110:111], off offset:128
	s_nop 0
	global_load_dwordx4 v[114:117], v[114:115], off offset:128
	s_nop 0
	global_load_dwordx4 v[86:89], v[86:87], off offset:128
	s_nop 0
	global_load_dwordx4 v[90:93], v[90:91], off offset:128
	s_nop 0
	global_load_dwordx4 v[94:97], v[94:95], off offset:128
	s_nop 0
	global_load_dwordx4 v[98:101], v[98:99], off offset:128
	s_cmp_eq_u32 s34, 0
	s_cselect_b64 s[30:31], -1, 0
	s_cmp_lg_u32 s34, 0
	s_cbranch_scc1 .LBB0_722
	v_mov_b32_e32 v244, 0
	v_mov_b32_e32 v202, 0xf149f2ca
	v_mov_b32_e32 v154, 0
	v_mov_b32_e32 v155, v244
	v_mov_b32_e32 v156, v244
	v_mov_b32_e32 v157, v244
	v_mov_b32_e32 v158, 0
	v_mov_b32_e32 v159, v244
	v_mov_b32_e32 v160, v244
	v_mov_b32_e32 v161, v244
	v_mov_b32_e32 v162, 0
	v_mov_b32_e32 v163, v244
	v_mov_b32_e32 v164, v244
	v_mov_b32_e32 v165, v244
	v_mov_b32_e32 v166, 0
	v_mov_b32_e32 v167, v244
	v_mov_b32_e32 v168, v244
	v_mov_b32_e32 v169, v244
.LBB0_722:
	s_add_i32 s42, s42, s49
	s_cmpk_gt_i32 s42, 0xfe
	s_cselect_b64 s[40:41], -1, 0
	s_cmpk_lt_i32 s42, 0xff
	s_mov_b32 s12, 0
	s_cbranch_scc1 .LBB0_724
	s_movk_i32 s12, 0x7e
	v_sub_u32_e32 v0, s42, v200
	v_cmp_lt_i32_e32 vcc, s12, v0
	s_and_b32 s12, vcc_lo, 1
.LBB0_724:
	v_mov_b64_e32 v[152:153], v[6:7]
	s_cmp_eq_u32 s12, 0
	v_mov_b64_e32 v[150:151], v[4:5]
	v_mov_b32_e32 v152, v4
	s_cbranch_scc1 .LBB0_726
	v_mov_b64_e32 v[172:173], v[152:153]
	v_mov_b64_e32 v[170:171], v[150:151]
	v_mov_b32_e32 v173, v4
	s_mov_b64 s[12:13], 0
	s_branch .LBB0_727

.LBB0_746:
	s_andn2_b64 vcc, exec, s[40:41]
	s_mov_b32 s12, 0
	s_cbranch_vccnz .LBB0_748
	s_movk_i32 s12, 0x7e
	v_sub_u32_e32 v0, s42, v201
	v_cmp_lt_i32_e32 vcc, s12, v0
	s_and_b32 s12, vcc_lo, 1
.LBB0_748:
	s_cmp_eq_u32 s12, 0
	s_cbranch_scc1 .LBB0_750
	v_mov_b32_e32 v153, v4
	s_mov_b64 s[12:13], 0
	s_branch .LBB0_751
